# v55 + P4 score sums via v_pk_add_f32 (pass1 in-loop bodies rewritten in-place med3 + packed adds across adjacent scores, pass2 adds packed); bitwise-identical f32 sums
# baseline (speedup 1.0000x reference)
; __device__ __forceinline__ int crow(int reg, int h) { return (reg & 3) + 8 * (reg >> 2) + 4 * h; }
; __device__ __forceinline__ int bin2(float sv, int zi) {
;     const unsigned u = __float_as_uint(sv);
;     int c = (int)((u >> 20) & 0x7FFu) - 832;
;     c = c < 0 ? 0 : (c > 207 ? 207 : c);
;     int b = (u >> 31) ? (207 - c) : (272 + c);
;     if (sv == 0.0f) b = 208 + zi;
;     return b;
; template <int STAGE>
; __device__ __forceinline__ void pass2(LAS unsigned char* lds, const bf16* kbase, int g, int t0, const bf16x8 (&qf)[4][4], const f32x4 lo4, const f32x4 hi4, int wave, int r, int h2) {
;     ...
;         f32x16 acc[4];
; #pragma unroll
;         for (int hd = 0; hd < 4; ++hd) {
;             acc[hd] = f32x16{};
; #pragma unroll
;             for (int s = 0; s < 4; ++s) acc[hd] = __builtin_amdgcn_mfma_f32_32x32x16_bf16(WN ? kn[s] : kf[s], qf[hd][s], acc[hd], 0, 0, 0);
;         }
;         const int zi = (8191 - 32 * kt) >> 7;
;         const int lim = tq - 32 * kt - 4 * h2;
;         unsigned gtw = 0u, eqw = 0u;
;         float svq[16];
; #pragma unroll
;         for (int rg = 0; rg < 16; ++rg) {
;             const int c0 = att::crow(rg, 0);
;             float sv = fsum4_s(__builtin_amdgcn_fmed3f(acc[0][rg], lo4.x, hi4.x), __builtin_amdgcn_fmed3f(acc[1][rg], lo4.y, hi4.y),
;                                __builtin_amdgcn_fmed3f(acc[2][rg], lo4.z, hi4.z), __builtin_amdgcn_fmed3f(acc[3][rg], lo4.w, hi4.w));
;             const int b = bin2(sv, zi);
;             const bool valid = !DIAG || c0 <= lim;
;             if (STAGE == 0) {
;                 atomicAdd((unsigned*)&hist[r * HROW2 + (valid ? b : NB2)], 1u);
.LBB0_787:
	s_add_i32 s4, s0, s1
	s_cmp_lg_u32 s4, 16
	s_cbranch_scc0 .LBB0_793
	s_waitcnt vmcnt(3)
	v_mfma_f32_32x32x16_bf16 v[0:15], v[140:143], v[64:67], 0
	s_lshr_b32 s4, s6, 7
	s_addk_i32 s4, 0xd0
	v_mfma_f32_32x32x16_bf16 v[16:31], v[140:143], v[80:83], 0
	v_mfma_f32_32x32x16_bf16 v[32:47], v[140:143], v[96:99], 0
	v_mfma_f32_32x32x16_bf16 v[48:63], v[140:143], v[112:115], 0
	s_waitcnt vmcnt(2)
	v_mfma_f32_32x32x16_bf16 v[0:15], v[136:139], v[68:71], v[0:15]
	v_mfma_f32_32x32x16_bf16 v[16:31], v[136:139], v[84:87], v[16:31]
	v_mfma_f32_32x32x16_bf16 v[32:47], v[136:139], v[100:103], v[32:47]
	v_mfma_f32_32x32x16_bf16 v[48:63], v[136:139], v[116:119], v[48:63]
	s_waitcnt vmcnt(1)
	v_mfma_f32_32x32x16_bf16 v[0:15], v[132:135], v[72:75], v[0:15]
	v_mfma_f32_32x32x16_bf16 v[16:31], v[132:135], v[88:91], v[16:31]
	v_mfma_f32_32x32x16_bf16 v[32:47], v[132:135], v[104:107], v[32:47]
	v_mfma_f32_32x32x16_bf16 v[48:63], v[132:135], v[120:123], v[48:63]
	s_waitcnt vmcnt(0)
	v_mfma_f32_32x32x16_bf16 v[0:15], v[128:131], v[76:79], v[0:15]
	v_mfma_f32_32x32x16_bf16 v[16:31], v[128:131], v[92:95], v[16:31]
	s_nop 10
	v_med3_f32 v0, v0, v207, v208
	v_med3_f32 v1, v1, v207, v208
	v_med3_f32 v2, v2, v207, v208
	v_med3_f32 v3, v3, v207, v208
	v_med3_f32 v4, v4, v207, v208
	v_med3_f32 v5, v5, v207, v208
	v_med3_f32 v6, v6, v207, v208
	v_med3_f32 v7, v7, v207, v208
	v_med3_f32 v8, v8, v207, v208
	v_med3_f32 v9, v9, v207, v208
	v_med3_f32 v10, v10, v207, v208
	v_med3_f32 v11, v11, v207, v208
	v_med3_f32 v12, v12, v207, v208
	v_med3_f32 v13, v13, v207, v208
	v_med3_f32 v14, v14, v207, v208
	v_med3_f32 v15, v15, v207, v208
	v_mfma_f32_32x32x16_bf16 v[32:47], v[128:131], v[108:111], v[32:47]
	v_med3_f32 v16, v16, v209, v210
	v_med3_f32 v17, v17, v209, v210
	v_med3_f32 v18, v18, v209, v210
	v_med3_f32 v19, v19, v209, v210
	v_med3_f32 v20, v20, v209, v210
	v_med3_f32 v21, v21, v209, v210
	v_med3_f32 v22, v22, v209, v210
	v_med3_f32 v23, v23, v209, v210
	v_med3_f32 v24, v24, v209, v210
	v_med3_f32 v25, v25, v209, v210
	v_med3_f32 v26, v26, v209, v210
	v_med3_f32 v27, v27, v209, v210
	v_med3_f32 v28, v28, v209, v210
	v_med3_f32 v29, v29, v209, v210
	v_med3_f32 v30, v30, v209, v210
	v_med3_f32 v31, v31, v209, v210
	v_mfma_f32_32x32x16_bf16 v[48:63], v[128:131], v[124:127], v[48:63]
	v_mov_b32_e32 v162, s4
	s_mov_b64 s[4:5], -1
	v_med3_f32 v32, v32, v212, v213
	v_med3_f32 v33, v33, v212, v213
	v_med3_f32 v34, v34, v212, v213
	v_med3_f32 v35, v35, v212, v213
	v_med3_f32 v36, v36, v212, v213
	v_med3_f32 v37, v37, v212, v213
	v_med3_f32 v38, v38, v212, v213
	v_med3_f32 v39, v39, v212, v213
	v_med3_f32 v40, v40, v212, v213
	v_med3_f32 v41, v41, v212, v213
	v_med3_f32 v42, v42, v212, v213
	v_med3_f32 v43, v43, v212, v213
	v_med3_f32 v44, v44, v212, v213
	v_med3_f32 v45, v45, v212, v213
	v_med3_f32 v46, v46, v212, v213
	v_med3_f32 v47, v47, v212, v213
	v_med3_f32 v48, v48, v214, v215
	v_med3_f32 v49, v49, v214, v215
	v_med3_f32 v50, v50, v214, v215
	v_med3_f32 v51, v51, v214, v215
	v_med3_f32 v52, v52, v214, v215
	v_med3_f32 v53, v53, v214, v215
	v_med3_f32 v54, v54, v214, v215
	v_med3_f32 v55, v55, v214, v215
	v_med3_f32 v56, v56, v214, v215
	v_med3_f32 v57, v57, v214, v215
	v_med3_f32 v58, v58, v214, v215
	v_med3_f32 v59, v59, v214, v215
	v_med3_f32 v60, v60, v214, v215
	v_med3_f32 v61, v61, v214, v215
	v_med3_f32 v62, v62, v214, v215
	v_med3_f32 v63, v63, v214, v215
	v_pk_add_f32 v[0:1], v[0:1], v[16:17]
	v_pk_add_f32 v[32:33], v[32:33], v[48:49]
	v_pk_add_f32 v[2:3], v[2:3], v[18:19]
	v_pk_add_f32 v[34:35], v[34:35], v[50:51]
	v_pk_add_f32 v[4:5], v[4:5], v[20:21]
	v_pk_add_f32 v[36:37], v[36:37], v[52:53]
	v_pk_add_f32 v[6:7], v[6:7], v[22:23]
	v_pk_add_f32 v[38:39], v[38:39], v[54:55]
	v_pk_add_f32 v[8:9], v[8:9], v[24:25]
	v_pk_add_f32 v[40:41], v[40:41], v[56:57]
	v_pk_add_f32 v[10:11], v[10:11], v[26:27]
	v_pk_add_f32 v[42:43], v[42:43], v[58:59]
	v_pk_add_f32 v[12:13], v[12:13], v[28:29]
	v_pk_add_f32 v[44:45], v[44:45], v[60:61]
	v_pk_add_f32 v[14:15], v[14:15], v[30:31]
	v_pk_add_f32 v[46:47], v[46:47], v[62:63]
	v_pk_add_f32 v[0:1], v[0:1], v[32:33]
	v_pk_add_f32 v[2:3], v[2:3], v[34:35]
	v_pk_add_f32 v[4:5], v[4:5], v[36:37]
	v_pk_add_f32 v[6:7], v[6:7], v[38:39]
	v_pk_add_f32 v[8:9], v[8:9], v[40:41]
	v_pk_add_f32 v[10:11], v[10:11], v[42:43]
	v_pk_add_f32 v[12:13], v[12:13], v[44:45]
	v_pk_add_f32 v[14:15], v[14:15], v[46:47]
	v_bfe_u32 v16, v0, 20, 11
	v_bfe_u32 v18, v1, 20, 11
	v_cmp_gt_i32_e32 vcc, 0, v0
	v_cmp_gt_i32_e64 s[98:99], 0, v1
	v_med3_u32 v16, v16, s91, v190
	v_med3_u32 v18, v18, s91, v190
	v_sub_u32_e32 v17, 0x40f, v16
	v_add_u32_e32 v16, 0xfffffdd0, v16
	v_sub_u32_e32 v19, 0x40f, v18
	v_add_u32_e32 v18, 0xfffffdd0, v18
	v_cndmask_b32_e32 v16, v16, v17, vcc
	v_cmp_eq_f32_e32 vcc, 0, v0
	v_cndmask_b32_e64 v18, v18, v19, s[98:99]
	v_cmp_eq_f32_e64 s[98:99], 0, v1
	v_cndmask_b32_e32 v16, v16, v162, vcc
	v_lshl_add_u32 v16, v16, 2, v204
	v_cndmask_b32_e64 v18, v18, v162, s[98:99]
	ds_add_u32 v16, v184
	v_lshl_add_u32 v18, v18, 2, v204
	ds_add_u32 v18, v184
	v_bfe_u32 v20, v2, 20, 11
	v_bfe_u32 v22, v3, 20, 11
	v_cmp_gt_i32_e32 vcc, 0, v2
	v_cmp_gt_i32_e64 s[98:99], 0, v3
	v_med3_u32 v20, v20, s91, v190
	v_med3_u32 v22, v22, s91, v190
	v_sub_u32_e32 v21, 0x40f, v20
	v_add_u32_e32 v20, 0xfffffdd0, v20
	v_sub_u32_e32 v23, 0x40f, v22
	v_add_u32_e32 v22, 0xfffffdd0, v22
	v_cndmask_b32_e32 v20, v20, v21, vcc
	v_cmp_eq_f32_e32 vcc, 0, v2
	v_cndmask_b32_e64 v22, v22, v23, s[98:99]
	v_cmp_eq_f32_e64 s[98:99], 0, v3
	v_cndmask_b32_e32 v20, v20, v162, vcc
	v_lshl_add_u32 v20, v20, 2, v204
	v_cndmask_b32_e64 v22, v22, v162, s[98:99]
	ds_add_u32 v20, v184
; __device__ __forceinline__ int crow(int reg, int h) { return (reg & 3) + 8 * (reg >> 2) + 4 * h; }
; #define DSA2_LOADK(dst, kt_) do { _Pragma("unroll") for (int s = 0; s < 4; ++s) dst[s] = *(const bf16x8*)(kp + (size_t)(32 * (kt_)) * Y0P + 16 * s); } while (0)
; template <int STAGE>
; __device__ __forceinline__ void pass2(LAS unsigned char* lds, const bf16* kbase, int g, int t0, const bf16x8 (&qf)[4][4], const f32x4 lo4, const f32x4 hi4, int wave, int r, int h2) {
;     ...
;         for (int rg = 0; rg < 16; ++rg) {
;             const int c0 = att::crow(rg, 0);
;             float sv = fsum4_s(__builtin_amdgcn_fmed3f(acc[0][rg], lo4.x, hi4.x), __builtin_amdgcn_fmed3f(acc[1][rg], lo4.y, hi4.y),
;                                __builtin_amdgcn_fmed3f(acc[2][rg], lo4.z, hi4.z), __builtin_amdgcn_fmed3f(acc[3][rg], lo4.w, hi4.w));
;             const int b = bin2(sv, zi);
;             const bool valid = !DIAG || c0 <= lim;
;             if (STAGE == 0) {
;                 atomicAdd((unsigned*)&hist[r * HROW2 + (valid ? b : NB2)], 1u);
;             } else {
;     ...
;     int kt = wave;
;     if (kt <= g) DSA2_LOADK(kf, kt);
;     for (;;) {
;         if (kt > g) break;
;         if (kt + 8 <= g) DSA2_LOADK(kn, kt + 8);
;         if (kt == g) { tile(pg8::BoolC2<false>{}, kt, pg8::BoolC2<true>{}); break; }
;         tile(pg8::BoolC2<false>{}, kt, pg8::BoolC2<false>{});
;         kt += 8;
;         if (kt > g) break;
;         if (kt + 8 <= g) DSA2_LOADK(kf, kt + 8);
	v_lshl_add_u32 v22, v22, 2, v204
	ds_add_u32 v22, v184
	v_bfe_u32 v24, v4, 20, 11
	v_bfe_u32 v26, v5, 20, 11
	v_cmp_gt_i32_e32 vcc, 0, v4
	v_cmp_gt_i32_e64 s[98:99], 0, v5
	v_med3_u32 v24, v24, s91, v190
	v_med3_u32 v26, v26, s91, v190
	v_sub_u32_e32 v25, 0x40f, v24
	v_add_u32_e32 v24, 0xfffffdd0, v24
	v_sub_u32_e32 v27, 0x40f, v26
	v_add_u32_e32 v26, 0xfffffdd0, v26
	v_cndmask_b32_e32 v24, v24, v25, vcc
	v_cmp_eq_f32_e32 vcc, 0, v4
	v_cndmask_b32_e64 v26, v26, v27, s[98:99]
	v_cmp_eq_f32_e64 s[98:99], 0, v5
	v_cndmask_b32_e32 v24, v24, v162, vcc
	v_lshl_add_u32 v24, v24, 2, v204
	v_cndmask_b32_e64 v26, v26, v162, s[98:99]
	ds_add_u32 v24, v184
	v_lshl_add_u32 v26, v26, 2, v204
	ds_add_u32 v26, v184
	v_bfe_u32 v28, v6, 20, 11
	v_bfe_u32 v30, v7, 20, 11
	v_cmp_gt_i32_e32 vcc, 0, v6
	v_cmp_gt_i32_e64 s[98:99], 0, v7
	v_med3_u32 v28, v28, s91, v190
	v_med3_u32 v30, v30, s91, v190
	v_sub_u32_e32 v29, 0x40f, v28
	v_add_u32_e32 v28, 0xfffffdd0, v28
	v_sub_u32_e32 v31, 0x40f, v30
	v_add_u32_e32 v30, 0xfffffdd0, v30
	v_cndmask_b32_e32 v28, v28, v29, vcc
	v_cmp_eq_f32_e32 vcc, 0, v6
	v_cndmask_b32_e64 v30, v30, v31, s[98:99]
	v_cmp_eq_f32_e64 s[98:99], 0, v7
	v_cndmask_b32_e32 v28, v28, v162, vcc
	v_lshl_add_u32 v28, v28, 2, v204
	v_cndmask_b32_e64 v30, v30, v162, s[98:99]
	ds_add_u32 v28, v184
	v_lshl_add_u32 v30, v30, 2, v204
	ds_add_u32 v30, v184
	v_bfe_u32 v16, v8, 20, 11
	v_bfe_u32 v18, v9, 20, 11
	v_cmp_gt_i32_e32 vcc, 0, v8
	v_cmp_gt_i32_e64 s[98:99], 0, v9
	v_med3_u32 v16, v16, s91, v190
	v_med3_u32 v18, v18, s91, v190
	v_sub_u32_e32 v17, 0x40f, v16
	v_add_u32_e32 v16, 0xfffffdd0, v16
	v_sub_u32_e32 v19, 0x40f, v18
	v_add_u32_e32 v18, 0xfffffdd0, v18
	v_cndmask_b32_e32 v16, v16, v17, vcc
	v_cmp_eq_f32_e32 vcc, 0, v8
	v_cndmask_b32_e64 v18, v18, v19, s[98:99]
	v_cmp_eq_f32_e64 s[98:99], 0, v9
	v_cndmask_b32_e32 v16, v16, v162, vcc
	v_lshl_add_u32 v16, v16, 2, v204
	v_cndmask_b32_e64 v18, v18, v162, s[98:99]
	ds_add_u32 v16, v184
	v_lshl_add_u32 v18, v18, 2, v204
	ds_add_u32 v18, v184
	v_bfe_u32 v20, v10, 20, 11
	v_bfe_u32 v22, v11, 20, 11
	v_cmp_gt_i32_e32 vcc, 0, v10
	v_cmp_gt_i32_e64 s[98:99], 0, v11
	v_med3_u32 v20, v20, s91, v190
	v_med3_u32 v22, v22, s91, v190
	v_sub_u32_e32 v21, 0x40f, v20
	v_add_u32_e32 v20, 0xfffffdd0, v20
	v_sub_u32_e32 v23, 0x40f, v22
	v_add_u32_e32 v22, 0xfffffdd0, v22
	v_cndmask_b32_e32 v20, v20, v21, vcc
	v_cmp_eq_f32_e32 vcc, 0, v10
	v_cndmask_b32_e64 v22, v22, v23, s[98:99]
	v_cmp_eq_f32_e64 s[98:99], 0, v11
	v_cndmask_b32_e32 v20, v20, v162, vcc
	v_lshl_add_u32 v20, v20, 2, v204
	v_cndmask_b32_e64 v22, v22, v162, s[98:99]
	ds_add_u32 v20, v184
	v_lshl_add_u32 v22, v22, 2, v204
	ds_add_u32 v22, v184
	v_bfe_u32 v24, v12, 20, 11
	v_bfe_u32 v26, v13, 20, 11
	v_cmp_gt_i32_e32 vcc, 0, v12
	v_cmp_gt_i32_e64 s[98:99], 0, v13
	v_med3_u32 v24, v24, s91, v190
	v_med3_u32 v26, v26, s91, v190
	v_sub_u32_e32 v25, 0x40f, v24
	v_add_u32_e32 v24, 0xfffffdd0, v24
	v_sub_u32_e32 v27, 0x40f, v26
	v_add_u32_e32 v26, 0xfffffdd0, v26
	v_cndmask_b32_e32 v24, v24, v25, vcc
	v_cmp_eq_f32_e32 vcc, 0, v12
	v_cndmask_b32_e64 v26, v26, v27, s[98:99]
	v_cmp_eq_f32_e64 s[98:99], 0, v13
	v_cndmask_b32_e32 v24, v24, v162, vcc
	v_lshl_add_u32 v24, v24, 2, v204
	v_cndmask_b32_e64 v26, v26, v162, s[98:99]
	ds_add_u32 v24, v184
	v_lshl_add_u32 v26, v26, 2, v204
	ds_add_u32 v26, v184
	v_bfe_u32 v28, v14, 20, 11
	v_bfe_u32 v30, v15, 20, 11
	v_cmp_gt_i32_e32 vcc, 0, v14
	v_cmp_gt_i32_e64 s[98:99], 0, v15
	v_med3_u32 v28, v28, s91, v190
	v_med3_u32 v30, v30, s91, v190
	v_sub_u32_e32 v29, 0x40f, v28
	v_add_u32_e32 v28, 0xfffffdd0, v28
	v_sub_u32_e32 v31, 0x40f, v30
	v_add_u32_e32 v30, 0xfffffdd0, v30
	v_cndmask_b32_e32 v28, v28, v29, vcc
	v_cmp_eq_f32_e32 vcc, 0, v14
	v_cndmask_b32_e64 v30, v30, v31, s[98:99]
	v_cmp_eq_f32_e64 s[98:99], 0, v15
	v_cndmask_b32_e32 v28, v28, v162, vcc
	v_lshl_add_u32 v28, v28, 2, v204
	v_cndmask_b32_e64 v30, v30, v162, s[98:99]
	ds_add_u32 v28, v184
	v_lshl_add_u32 v30, v30, 2, v204
	ds_add_u32 v30, v184
	s_and_b64 vcc, exec, s[2:3]
	s_mov_b64 s[2:3], -1
	s_cbranch_vccz .LBB0_794
	s_cmp_gt_u32 s1, s64
	s_cselect_b64 s[2:3], -1, 0
	s_and_b64 vcc, exec, s[2:3]
	s_cbranch_vccnz .LBB0_791
	global_load_dwordx4 v[140:143], v[180:181], off offset:-96
	global_load_dwordx4 v[136:139], v[180:181], off offset:-64
	global_load_dwordx4 v[132:135], v[180:181], off offset:-32
	global_load_dwordx4 v[128:131], v[180:181], off
; __device__ __forceinline__ int crow(int reg, int h) { return (reg & 3) + 8 * (reg >> 2) + 4 * h; }
; #define DSA2_LOADK(dst, kt_) do { _Pragma("unroll") for (int s = 0; s < 4; ++s) dst[s] = *(const bf16x8*)(kp + (size_t)(32 * (kt_)) * Y0P + 16 * s); } while (0)
; template <int STAGE>
; __device__ __forceinline__ void pass2(LAS unsigned char* lds, const bf16* kbase, int g, int t0, const bf16x8 (&qf)[4][4], const f32x4 lo4, const f32x4 hi4, int wave, int r, int h2) {
;     ...
;         f32x16 acc[4];
; #pragma unroll
;         for (int hd = 0; hd < 4; ++hd) {
;             acc[hd] = f32x16{};
; #pragma unroll
;             for (int s = 0; s < 4; ++s) acc[hd] = __builtin_amdgcn_mfma_f32_32x32x16_bf16(WN ? kn[s] : kf[s], qf[hd][s], acc[hd], 0, 0, 0);
;         }
;         const int zi = (8191 - 32 * kt) >> 7;
;         const int lim = tq - 32 * kt - 4 * h2;
;         unsigned gtw = 0u, eqw = 0u;
;         float svq[16];
; #pragma unroll
;         for (int rg = 0; rg < 16; ++rg) {
;             const int c0 = att::crow(rg, 0);
;             float sv = fsum4_s(__builtin_amdgcn_fmed3f(acc[0][rg], lo4.x, hi4.x), __builtin_amdgcn_fmed3f(acc[1][rg], lo4.y, hi4.y),
;                                __builtin_amdgcn_fmed3f(acc[2][rg], lo4.z, hi4.z), __builtin_amdgcn_fmed3f(acc[3][rg], lo4.w, hi4.w));
;             const int b = bin2(sv, zi);
;             const bool valid = !DIAG || c0 <= lim;
;             if (STAGE == 0) {
;                 atomicAdd((unsigned*)&hist[r * HROW2 + (valid ? b : NB2)], 1u);
;     ...
;         tile(pg8::BoolC2<false>{}, kt, pg8::BoolC2<false>{});
;         kt += 8;
;         if (kt > g) break;
;         if (kt + 8 <= g) DSA2_LOADK(kf, kt + 8);
;         if (kt == g) { tile(pg8::BoolC2<true>{}, kt, pg8::BoolC2<true>{}); break; }
;         tile(pg8::BoolC2<true>{}, kt, pg8::BoolC2<false>{});
;         kt += 8;
.LBB0_791:
	s_add_i32 s1, s1, 16
	s_add_i32 s4, s0, s1
	s_cmp_lg_u32 s4, 24
	s_cbranch_scc0 .LBB0_795
	v_mfma_f32_32x32x16_bf16 v[0:15], v[156:159], v[64:67], 0
	s_add_i32 s4, s6, 0xffffff00
	s_lshr_b32 s4, s4, 7
	s_addk_i32 s4, 0xd0
	s_addk_i32 s6, 0xfe00
	s_mov_b64 s[8:9], 0
	v_mfma_f32_32x32x16_bf16 v[16:31], v[156:159], v[80:83], 0
	v_mfma_f32_32x32x16_bf16 v[32:47], v[156:159], v[96:99], 0
	v_mfma_f32_32x32x16_bf16 v[48:63], v[156:159], v[112:115], 0
	v_mfma_f32_32x32x16_bf16 v[0:15], v[152:155], v[68:71], v[0:15]
	v_mfma_f32_32x32x16_bf16 v[16:31], v[152:155], v[84:87], v[16:31]
	v_mfma_f32_32x32x16_bf16 v[32:47], v[152:155], v[100:103], v[32:47]
	v_mfma_f32_32x32x16_bf16 v[48:63], v[152:155], v[116:119], v[48:63]
	v_mfma_f32_32x32x16_bf16 v[0:15], v[148:151], v[72:75], v[0:15]
	v_mfma_f32_32x32x16_bf16 v[16:31], v[148:151], v[88:91], v[16:31]
	v_mfma_f32_32x32x16_bf16 v[32:47], v[148:151], v[104:107], v[32:47]
	v_mfma_f32_32x32x16_bf16 v[48:63], v[148:151], v[120:123], v[48:63]
	v_mfma_f32_32x32x16_bf16 v[0:15], v[144:147], v[76:79], v[0:15]
	v_mfma_f32_32x32x16_bf16 v[16:31], v[144:147], v[92:95], v[16:31]
	s_nop 10
	v_med3_f32 v0, v0, v207, v208
	v_med3_f32 v1, v1, v207, v208
	v_med3_f32 v2, v2, v207, v208
	v_med3_f32 v3, v3, v207, v208
	v_med3_f32 v4, v4, v207, v208
	v_med3_f32 v5, v5, v207, v208
	v_med3_f32 v6, v6, v207, v208
	v_med3_f32 v7, v7, v207, v208
	v_med3_f32 v8, v8, v207, v208
	v_med3_f32 v9, v9, v207, v208
	v_med3_f32 v10, v10, v207, v208
	v_med3_f32 v11, v11, v207, v208
	v_med3_f32 v12, v12, v207, v208
	v_med3_f32 v13, v13, v207, v208
	v_med3_f32 v14, v14, v207, v208
	v_med3_f32 v15, v15, v207, v208
	v_mfma_f32_32x32x16_bf16 v[32:47], v[144:147], v[108:111], v[32:47]
	v_med3_f32 v16, v16, v209, v210
	v_med3_f32 v17, v17, v209, v210
	v_med3_f32 v18, v18, v209, v210
	v_med3_f32 v19, v19, v209, v210
	v_med3_f32 v20, v20, v209, v210
	v_med3_f32 v21, v21, v209, v210
	v_med3_f32 v22, v22, v209, v210
	v_med3_f32 v23, v23, v209, v210
	v_med3_f32 v24, v24, v209, v210
	v_med3_f32 v25, v25, v209, v210
	v_med3_f32 v26, v26, v209, v210
	v_med3_f32 v27, v27, v209, v210
	v_med3_f32 v28, v28, v209, v210
	v_med3_f32 v29, v29, v209, v210
	v_med3_f32 v30, v30, v209, v210
	v_med3_f32 v31, v31, v209, v210
	v_mfma_f32_32x32x16_bf16 v[48:63], v[144:147], v[124:127], v[48:63]
	v_mov_b32_e32 v162, s4
	s_mov_b64 s[4:5], 0x380000
	v_lshl_add_u64 v[180:181], v[180:181], 0, s[4:5]
	s_mov_b64 s[4:5], -1
	v_med3_f32 v32, v32, v212, v213
	v_med3_f32 v33, v33, v212, v213
	v_med3_f32 v34, v34, v212, v213
	v_med3_f32 v35, v35, v212, v213
	v_med3_f32 v36, v36, v212, v213
	v_med3_f32 v37, v37, v212, v213
	v_med3_f32 v38, v38, v212, v213
	v_med3_f32 v39, v39, v212, v213
	v_med3_f32 v40, v40, v212, v213
	v_med3_f32 v41, v41, v212, v213
	v_med3_f32 v42, v42, v212, v213
	v_med3_f32 v43, v43, v212, v213
	v_med3_f32 v44, v44, v212, v213
	v_med3_f32 v45, v45, v212, v213
	v_med3_f32 v46, v46, v212, v213
	v_med3_f32 v47, v47, v212, v213
	v_med3_f32 v48, v48, v214, v215
	v_med3_f32 v49, v49, v214, v215
	v_med3_f32 v50, v50, v214, v215
	v_med3_f32 v51, v51, v214, v215
	v_med3_f32 v52, v52, v214, v215
	v_med3_f32 v53, v53, v214, v215
	v_med3_f32 v54, v54, v214, v215
	v_med3_f32 v55, v55, v214, v215
	v_med3_f32 v56, v56, v214, v215
	v_med3_f32 v57, v57, v214, v215
	v_med3_f32 v58, v58, v214, v215
	v_med3_f32 v59, v59, v214, v215
	v_med3_f32 v60, v60, v214, v215
	v_med3_f32 v61, v61, v214, v215
	v_med3_f32 v62, v62, v214, v215
	v_med3_f32 v63, v63, v214, v215
	v_pk_add_f32 v[0:1], v[0:1], v[16:17]
	v_pk_add_f32 v[32:33], v[32:33], v[48:49]
	v_pk_add_f32 v[2:3], v[2:3], v[18:19]
	v_pk_add_f32 v[34:35], v[34:35], v[50:51]
	v_pk_add_f32 v[4:5], v[4:5], v[20:21]
	v_pk_add_f32 v[36:37], v[36:37], v[52:53]
	v_pk_add_f32 v[6:7], v[6:7], v[22:23]
	v_pk_add_f32 v[38:39], v[38:39], v[54:55]
	v_pk_add_f32 v[8:9], v[8:9], v[24:25]
	v_pk_add_f32 v[40:41], v[40:41], v[56:57]
	v_pk_add_f32 v[10:11], v[10:11], v[26:27]
	v_pk_add_f32 v[42:43], v[42:43], v[58:59]
	v_pk_add_f32 v[12:13], v[12:13], v[28:29]
	v_pk_add_f32 v[44:45], v[44:45], v[60:61]
	v_pk_add_f32 v[14:15], v[14:15], v[30:31]
	v_pk_add_f32 v[46:47], v[46:47], v[62:63]
	v_pk_add_f32 v[0:1], v[0:1], v[32:33]
	v_pk_add_f32 v[2:3], v[2:3], v[34:35]
	v_pk_add_f32 v[4:5], v[4:5], v[36:37]
	v_pk_add_f32 v[6:7], v[6:7], v[38:39]
	v_pk_add_f32 v[8:9], v[8:9], v[40:41]
	v_pk_add_f32 v[10:11], v[10:11], v[42:43]
	v_pk_add_f32 v[12:13], v[12:13], v[44:45]
	v_pk_add_f32 v[14:15], v[14:15], v[46:47]
	v_bfe_u32 v16, v0, 20, 11
	v_bfe_u32 v18, v1, 20, 11
	v_cmp_gt_i32_e32 vcc, 0, v0
	v_cmp_gt_i32_e64 s[98:99], 0, v1
	v_med3_u32 v16, v16, s91, v190
	v_med3_u32 v18, v18, s91, v190
	v_sub_u32_e32 v17, 0x40f, v16
	v_add_u32_e32 v16, 0xfffffdd0, v16
	v_sub_u32_e32 v19, 0x40f, v18
	v_add_u32_e32 v18, 0xfffffdd0, v18
	v_cndmask_b32_e32 v16, v16, v17, vcc
	v_cmp_eq_f32_e32 vcc, 0, v0
	v_cndmask_b32_e64 v18, v18, v19, s[98:99]
; __device__ __forceinline__ int crow(int reg, int h) { return (reg & 3) + 8 * (reg >> 2) + 4 * h; }
; template <int STAGE>
; __device__ __forceinline__ void pass2(LAS unsigned char* lds, const bf16* kbase, int g, int t0, const bf16x8 (&qf)[4][4], const f32x4 lo4, const f32x4 hi4, int wave, int r, int h2) {
;     ...
;         for (int rg = 0; rg < 16; ++rg) {
;             const int c0 = att::crow(rg, 0);
;             float sv = fsum4_s(__builtin_amdgcn_fmed3f(acc[0][rg], lo4.x, hi4.x), __builtin_amdgcn_fmed3f(acc[1][rg], lo4.y, hi4.y),
;                                __builtin_amdgcn_fmed3f(acc[2][rg], lo4.z, hi4.z), __builtin_amdgcn_fmed3f(acc[3][rg], lo4.w, hi4.w));
;             const int b = bin2(sv, zi);
;             const bool valid = !DIAG || c0 <= lim;
;             if (STAGE == 0) {
;                 atomicAdd((unsigned*)&hist[r * HROW2 + (valid ? b : NB2)], 1u);
;             } else {
	v_cmp_eq_f32_e64 s[98:99], 0, v1
	v_cndmask_b32_e32 v16, v16, v162, vcc
	v_lshl_add_u32 v16, v16, 2, v204
	v_cndmask_b32_e64 v18, v18, v162, s[98:99]
	ds_add_u32 v16, v184
	v_lshl_add_u32 v18, v18, 2, v204
	ds_add_u32 v18, v184
	v_bfe_u32 v20, v2, 20, 11
	v_bfe_u32 v22, v3, 20, 11
	v_cmp_gt_i32_e32 vcc, 0, v2
	v_cmp_gt_i32_e64 s[98:99], 0, v3
	v_med3_u32 v20, v20, s91, v190
	v_med3_u32 v22, v22, s91, v190
	v_sub_u32_e32 v21, 0x40f, v20
	v_add_u32_e32 v20, 0xfffffdd0, v20
	v_sub_u32_e32 v23, 0x40f, v22
	v_add_u32_e32 v22, 0xfffffdd0, v22
	v_cndmask_b32_e32 v20, v20, v21, vcc
	v_cmp_eq_f32_e32 vcc, 0, v2
	v_cndmask_b32_e64 v22, v22, v23, s[98:99]
	v_cmp_eq_f32_e64 s[98:99], 0, v3
	v_cndmask_b32_e32 v20, v20, v162, vcc
	v_lshl_add_u32 v20, v20, 2, v204
	v_cndmask_b32_e64 v22, v22, v162, s[98:99]
	ds_add_u32 v20, v184
	v_lshl_add_u32 v22, v22, 2, v204
	ds_add_u32 v22, v184
	v_bfe_u32 v24, v4, 20, 11
	v_bfe_u32 v26, v5, 20, 11
	v_cmp_gt_i32_e32 vcc, 0, v4
	v_cmp_gt_i32_e64 s[98:99], 0, v5
	v_med3_u32 v24, v24, s91, v190
	v_med3_u32 v26, v26, s91, v190
	v_sub_u32_e32 v25, 0x40f, v24
	v_add_u32_e32 v24, 0xfffffdd0, v24
	v_sub_u32_e32 v27, 0x40f, v26
	v_add_u32_e32 v26, 0xfffffdd0, v26
	v_cndmask_b32_e32 v24, v24, v25, vcc
	v_cmp_eq_f32_e32 vcc, 0, v4
	v_cndmask_b32_e64 v26, v26, v27, s[98:99]
	v_cmp_eq_f32_e64 s[98:99], 0, v5
	v_cndmask_b32_e32 v24, v24, v162, vcc
	v_lshl_add_u32 v24, v24, 2, v204
	v_cndmask_b32_e64 v26, v26, v162, s[98:99]
	ds_add_u32 v24, v184
	v_lshl_add_u32 v26, v26, 2, v204
	ds_add_u32 v26, v184
	v_bfe_u32 v28, v6, 20, 11
	v_bfe_u32 v30, v7, 20, 11
	v_cmp_gt_i32_e32 vcc, 0, v6
	v_cmp_gt_i32_e64 s[98:99], 0, v7
	v_med3_u32 v28, v28, s91, v190
	v_med3_u32 v30, v30, s91, v190
	v_sub_u32_e32 v29, 0x40f, v28
	v_add_u32_e32 v28, 0xfffffdd0, v28
	v_sub_u32_e32 v31, 0x40f, v30
	v_add_u32_e32 v30, 0xfffffdd0, v30
	v_cndmask_b32_e32 v28, v28, v29, vcc
	v_cmp_eq_f32_e32 vcc, 0, v6
	v_cndmask_b32_e64 v30, v30, v31, s[98:99]
	v_cmp_eq_f32_e64 s[98:99], 0, v7
	v_cndmask_b32_e32 v28, v28, v162, vcc
	v_lshl_add_u32 v28, v28, 2, v204
	v_cndmask_b32_e64 v30, v30, v162, s[98:99]
	ds_add_u32 v28, v184
	v_lshl_add_u32 v30, v30, 2, v204
	ds_add_u32 v30, v184
	v_bfe_u32 v16, v8, 20, 11
	v_bfe_u32 v18, v9, 20, 11
	v_cmp_gt_i32_e32 vcc, 0, v8
	v_cmp_gt_i32_e64 s[98:99], 0, v9
	v_med3_u32 v16, v16, s91, v190
	v_med3_u32 v18, v18, s91, v190
	v_sub_u32_e32 v17, 0x40f, v16
	v_add_u32_e32 v16, 0xfffffdd0, v16
	v_sub_u32_e32 v19, 0x40f, v18
	v_add_u32_e32 v18, 0xfffffdd0, v18
	v_cndmask_b32_e32 v16, v16, v17, vcc
	v_cmp_eq_f32_e32 vcc, 0, v8
	v_cndmask_b32_e64 v18, v18, v19, s[98:99]
	v_cmp_eq_f32_e64 s[98:99], 0, v9
	v_cndmask_b32_e32 v16, v16, v162, vcc
	v_lshl_add_u32 v16, v16, 2, v204
	v_cndmask_b32_e64 v18, v18, v162, s[98:99]
	ds_add_u32 v16, v184
	v_lshl_add_u32 v18, v18, 2, v204
	ds_add_u32 v18, v184
	v_bfe_u32 v20, v10, 20, 11
	v_bfe_u32 v22, v11, 20, 11
	v_cmp_gt_i32_e32 vcc, 0, v10
	v_cmp_gt_i32_e64 s[98:99], 0, v11
	v_med3_u32 v20, v20, s91, v190
	v_med3_u32 v22, v22, s91, v190
	v_sub_u32_e32 v21, 0x40f, v20
	v_add_u32_e32 v20, 0xfffffdd0, v20
	v_sub_u32_e32 v23, 0x40f, v22
	v_add_u32_e32 v22, 0xfffffdd0, v22
	v_cndmask_b32_e32 v20, v20, v21, vcc
	v_cmp_eq_f32_e32 vcc, 0, v10
	v_cndmask_b32_e64 v22, v22, v23, s[98:99]
	v_cmp_eq_f32_e64 s[98:99], 0, v11
	v_cndmask_b32_e32 v20, v20, v162, vcc
	v_lshl_add_u32 v20, v20, 2, v204
	v_cndmask_b32_e64 v22, v22, v162, s[98:99]
	ds_add_u32 v20, v184
	v_lshl_add_u32 v22, v22, 2, v204
	ds_add_u32 v22, v184
	v_bfe_u32 v24, v12, 20, 11
	v_bfe_u32 v26, v13, 20, 11
	v_cmp_gt_i32_e32 vcc, 0, v12
	v_cmp_gt_i32_e64 s[98:99], 0, v13
	v_med3_u32 v24, v24, s91, v190
	v_med3_u32 v26, v26, s91, v190
	v_sub_u32_e32 v25, 0x40f, v24
	v_add_u32_e32 v24, 0xfffffdd0, v24
	v_sub_u32_e32 v27, 0x40f, v26
	v_add_u32_e32 v26, 0xfffffdd0, v26
	v_cndmask_b32_e32 v24, v24, v25, vcc
	v_cmp_eq_f32_e32 vcc, 0, v12
	v_cndmask_b32_e64 v26, v26, v27, s[98:99]
	v_cmp_eq_f32_e64 s[98:99], 0, v13
	v_cndmask_b32_e32 v24, v24, v162, vcc
	v_lshl_add_u32 v24, v24, 2, v204
	v_cndmask_b32_e64 v26, v26, v162, s[98:99]
	ds_add_u32 v24, v184
	v_lshl_add_u32 v26, v26, 2, v204
	ds_add_u32 v26, v184
	v_bfe_u32 v28, v14, 20, 11
	v_bfe_u32 v30, v15, 20, 11
	v_cmp_gt_i32_e32 vcc, 0, v14
	v_cmp_gt_i32_e64 s[98:99], 0, v15
	v_med3_u32 v28, v28, s91, v190
	v_med3_u32 v30, v30, s91, v190
	v_sub_u32_e32 v29, 0x40f, v28
	v_add_u32_e32 v28, 0xfffffdd0, v28
	v_sub_u32_e32 v31, 0x40f, v30
	v_add_u32_e32 v30, 0xfffffdd0, v30
	v_cndmask_b32_e32 v28, v28, v29, vcc
	v_cmp_eq_f32_e32 vcc, 0, v14
	v_cndmask_b32_e64 v30, v30, v31, s[98:99]
	v_cmp_eq_f32_e64 s[98:99], 0, v15
	v_cndmask_b32_e32 v28, v28, v162, vcc
	v_lshl_add_u32 v28, v28, 2, v204
	v_cndmask_b32_e64 v30, v30, v162, s[98:99]
	ds_add_u32 v28, v184
	v_lshl_add_u32 v30, v30, 2, v204
	ds_add_u32 v30, v184
	s_and_b64 vcc, exec, s[2:3]
	s_cbranch_vccz .LBB0_796
	s_branch .LBB0_797

; template <int STAGE>
; __device__ __forceinline__ void pass2(LAS unsigned char* lds, const bf16* kbase, int g, int t0, const bf16x8 (&qf)[4][4], const f32x4 lo4, const f32x4 hi4, int wave, int r, int h2) {
;     ...
;         f32x16 acc[4];
; #pragma unroll
;         for (int hd = 0; hd < 4; ++hd) {
;             acc[hd] = f32x16{};
; #pragma unroll
;             for (int s = 0; s < 4; ++s) acc[hd] = __builtin_amdgcn_mfma_f32_32x32x16_bf16(WN ? kn[s] : kf[s], qf[hd][s], acc[hd], 0, 0, 0);
;         }
.LBB0_826:
	s_cmp_lg_u32 s0, s64
	s_cbranch_scc0 .LBB0_852
	s_waitcnt vmcnt(3)
	v_mfma_f32_32x32x16_bf16 v[0:15], v[140:143], v[64:67], 0
	s_lshl_b32 s6, s0, 5
	s_sub_i32 s7, 0x1fe0, s6
	s_lshr_b32 s7, s7, 7
	s_addk_i32 s7, 0xd0
	v_mfma_f32_32x32x16_bf16 v[16:31], v[140:143], v[80:83], 0
	v_mfma_f32_32x32x16_bf16 v[32:47], v[140:143], v[96:99], 0
	v_mfma_f32_32x32x16_bf16 v[48:63], v[140:143], v[112:115], 0
	s_waitcnt vmcnt(2)
	v_mfma_f32_32x32x16_bf16 v[0:15], v[136:139], v[68:71], v[0:15]
	v_mfma_f32_32x32x16_bf16 v[16:31], v[136:139], v[84:87], v[16:31]
	v_mfma_f32_32x32x16_bf16 v[32:47], v[136:139], v[100:103], v[32:47]
	v_mfma_f32_32x32x16_bf16 v[48:63], v[136:139], v[116:119], v[48:63]
	s_waitcnt vmcnt(1)
	v_mfma_f32_32x32x16_bf16 v[0:15], v[132:135], v[72:75], v[0:15]
	v_mfma_f32_32x32x16_bf16 v[16:31], v[132:135], v[88:91], v[16:31]
	v_mfma_f32_32x32x16_bf16 v[32:47], v[132:135], v[104:107], v[32:47]
	v_mfma_f32_32x32x16_bf16 v[48:63], v[132:135], v[120:123], v[48:63]
	s_waitcnt vmcnt(0)
; #define LAS __attribute__((address_space(3)))
; __device__ __forceinline__ int crow(int reg, int h) { return (reg & 3) + 8 * (reg >> 2) + 4 * h; }
; template <int STAGE>
; __device__ __forceinline__ void pass2(LAS unsigned char* lds, const bf16* kbase, int g, int t0, const bf16x8 (&qf)[4][4], const f32x4 lo4, const f32x4 hi4, int wave, int r, int h2) {
;     ...
;         for (int rg = 0; rg < 16; ++rg) {
;             const int c0 = att::crow(rg, 0);
;             float sv = fsum4_s(__builtin_amdgcn_fmed3f(acc[0][rg], lo4.x, hi4.x), __builtin_amdgcn_fmed3f(acc[1][rg], lo4.y, hi4.y),
;                                __builtin_amdgcn_fmed3f(acc[2][rg], lo4.z, hi4.z), __builtin_amdgcn_fmed3f(acc[3][rg], lo4.w, hi4.w));
;             const int b = bin2(sv, zi);
;             const bool valid = !DIAG || c0 <= lim;
;             if (STAGE == 0) {
;                 atomicAdd((unsigned*)&hist[r * HROW2 + (valid ? b : NB2)], 1u);
;             } else {
;                 if (valid && b > tb) gtw |= 1u << c0;
;                 if (valid && b == tb) eqw |= 1u << c0;
;                 svq[rg] = sv;
;             }
;         }
;         if (STAGE == 1) {
;             LAS unsigned char* st = lds + OFF2_SV + wave * 4096 + (r + 32 * h2) * 16;
; #pragma unroll
;             for (int q = 0; q < 4; ++q) *(LAS f32x4*)(st + q * 1024) = (f32x4){svq[4 * q], svq[4 * q + 1], svq[4 * q + 2], svq[4 * q + 3]};
	v_mfma_f32_32x32x16_bf16 v[0:15], v[128:131], v[76:79], v[0:15]
	v_mfma_f32_32x32x16_bf16 v[16:31], v[128:131], v[92:95], v[16:31]
	v_mfma_f32_32x32x16_bf16 v[32:47], v[128:131], v[108:111], v[32:47]
	v_mfma_f32_32x32x16_bf16 v[48:63], v[128:131], v[124:127], v[48:63]
	v_cmp_gt_i32_e32 vcc, s7, v232
	v_cmp_ge_i32_e64 s[98:99], s7, v232
	s_nop 6
	v_cndmask_b32_e32 v250, v252, v177, vcc
	v_cndmask_b32_e64 v251, v253, v177, s[98:99]
	v_med3_f32 v0, v0, v207, v208
	v_med3_f32 v1, v1, v207, v208
	v_med3_f32 v2, v2, v207, v208
	v_med3_f32 v3, v3, v207, v208
	v_med3_f32 v4, v4, v207, v208
	v_med3_f32 v5, v5, v207, v208
	v_med3_f32 v6, v6, v207, v208
	v_med3_f32 v7, v7, v207, v208
	v_med3_f32 v8, v8, v207, v208
	v_med3_f32 v9, v9, v207, v208
	v_med3_f32 v10, v10, v207, v208
	v_med3_f32 v11, v11, v207, v208
	v_med3_f32 v12, v12, v207, v208
	v_med3_f32 v13, v13, v207, v208
	v_med3_f32 v14, v14, v207, v208
	v_med3_f32 v15, v15, v207, v208
	v_med3_f32 v16, v16, v209, v210
	v_med3_f32 v17, v17, v209, v210
	v_med3_f32 v18, v18, v209, v210
	v_med3_f32 v19, v19, v209, v210
	v_med3_f32 v20, v20, v209, v210
	v_med3_f32 v21, v21, v209, v210
	v_med3_f32 v22, v22, v209, v210
	v_med3_f32 v23, v23, v209, v210
	v_med3_f32 v24, v24, v209, v210
	v_med3_f32 v25, v25, v209, v210
	v_med3_f32 v26, v26, v209, v210
	v_med3_f32 v27, v27, v209, v210
	v_med3_f32 v28, v28, v209, v210
	v_med3_f32 v29, v29, v209, v210
	v_med3_f32 v30, v30, v209, v210
	v_med3_f32 v31, v31, v209, v210
	v_med3_f32 v32, v32, v212, v213
	v_med3_f32 v33, v33, v212, v213
	v_med3_f32 v34, v34, v212, v213
	v_med3_f32 v35, v35, v212, v213
	v_med3_f32 v36, v36, v212, v213
	v_med3_f32 v37, v37, v212, v213
	v_med3_f32 v38, v38, v212, v213
	v_med3_f32 v39, v39, v212, v213
	v_med3_f32 v40, v40, v212, v213
	v_med3_f32 v41, v41, v212, v213
	v_med3_f32 v42, v42, v212, v213
	v_med3_f32 v43, v43, v212, v213
	v_med3_f32 v44, v44, v212, v213
	v_med3_f32 v45, v45, v212, v213
	v_med3_f32 v46, v46, v212, v213
	v_med3_f32 v47, v47, v212, v213
	v_med3_f32 v48, v48, v214, v215
	v_med3_f32 v49, v49, v214, v215
	v_med3_f32 v50, v50, v214, v215
	v_med3_f32 v51, v51, v214, v215
	v_med3_f32 v52, v52, v214, v215
	v_med3_f32 v53, v53, v214, v215
	v_med3_f32 v54, v54, v214, v215
	v_med3_f32 v55, v55, v214, v215
	v_med3_f32 v56, v56, v214, v215
	v_med3_f32 v57, v57, v214, v215
	v_med3_f32 v58, v58, v214, v215
	v_med3_f32 v59, v59, v214, v215
	v_med3_f32 v60, v60, v214, v215
	v_med3_f32 v61, v61, v214, v215
	v_med3_f32 v62, v62, v214, v215
	v_med3_f32 v63, v63, v214, v215
	v_pk_add_f32 v[0:1], v[0:1], v[16:17]
	v_pk_add_f32 v[32:33], v[32:33], v[48:49]
	v_pk_add_f32 v[234:235], v[0:1], v[32:33]
	v_pk_add_f32 v[2:3], v[2:3], v[18:19]
	v_pk_add_f32 v[34:35], v[34:35], v[50:51]
	v_pk_add_f32 v[236:237], v[2:3], v[34:35]
	v_pk_add_f32 v[4:5], v[4:5], v[20:21]
	v_pk_add_f32 v[36:37], v[36:37], v[52:53]
	v_pk_add_f32 v[238:239], v[4:5], v[36:37]
	v_pk_add_f32 v[6:7], v[6:7], v[22:23]
	v_pk_add_f32 v[38:39], v[38:39], v[54:55]
	v_pk_add_f32 v[240:241], v[6:7], v[38:39]
	v_pk_add_f32 v[8:9], v[8:9], v[24:25]
	v_pk_add_f32 v[40:41], v[40:41], v[56:57]
	v_pk_add_f32 v[242:243], v[8:9], v[40:41]
	v_pk_add_f32 v[10:11], v[10:11], v[26:27]
	v_pk_add_f32 v[42:43], v[42:43], v[58:59]
	v_pk_add_f32 v[244:245], v[10:11], v[42:43]
	v_pk_add_f32 v[12:13], v[12:13], v[28:29]
	v_pk_add_f32 v[44:45], v[44:45], v[60:61]
	v_pk_add_f32 v[246:247], v[12:13], v[44:45]
	v_pk_add_f32 v[14:15], v[14:15], v[30:31]
	v_pk_add_f32 v[46:47], v[46:47], v[62:63]
	v_pk_add_f32 v[248:249], v[14:15], v[46:47]
	v_cmp_ge_f32_e32 vcc, v234, v250
	v_cmp_ge_f32_e64 s[98:99], v234, v251
	v_cmp_ge_f32_e64 s[100:101], v235, v250
	v_cndmask_b32_e64 v0, 0, 1, vcc
	v_cmp_ge_f32_e32 vcc, v235, v251
	v_cndmask_b32_e64 v16, 0, 1, s[98:99]
	v_cmp_ge_f32_e64 s[98:99], v236, v250
	v_cndmask_b32_e64 v1, 0, 2, s[100:101]
	v_cmp_ge_f32_e64 s[100:101], v236, v251
	v_cndmask_b32_e64 v17, 0, 2, vcc
	v_cmp_ge_f32_e32 vcc, v237, v250
	v_cndmask_b32_e64 v2, 0, 4, s[98:99]
	v_cmp_ge_f32_e64 s[98:99], v237, v251
	v_cndmask_b32_e64 v18, 0, 4, s[100:101]
	v_cmp_ge_f32_e64 s[100:101], v238, v250
	v_cndmask_b32_e64 v3, 0, 8, vcc
	v_cmp_ge_f32_e32 vcc, v238, v251
	v_cndmask_b32_e64 v19, 0, 8, s[98:99]
	v_cmp_ge_f32_e64 s[98:99], v239, v250
	v_cndmask_b32_e64 v4, 0, v186, s[100:101]
	v_cmp_ge_f32_e64 s[100:101], v239, v251
	v_cndmask_b32_e64 v20, 0, v186, vcc
	v_cmp_ge_f32_e32 vcc, v240, v250
	v_cndmask_b32_e64 v5, 0, v193, s[98:99]
	v_cmp_ge_f32_e64 s[98:99], v240, v251
	v_cndmask_b32_e64 v21, 0, v193, s[100:101]
	v_cmp_ge_f32_e64 s[100:101], v241, v250
	v_cndmask_b32_e64 v6, 0, v194, vcc
	v_cmp_ge_f32_e32 vcc, v241, v251
	v_cndmask_b32_e64 v22, 0, v194, s[98:99]
	v_cmp_ge_f32_e64 s[98:99], v242, v250
	v_cndmask_b32_e64 v7, 0, v195, s[100:101]
	v_cmp_ge_f32_e64 s[100:101], v242, v251
	v_cndmask_b32_e64 v23, 0, v195, vcc
	v_cmp_ge_f32_e32 vcc, v243, v250
	v_cndmask_b32_e64 v8, 0, v196, s[98:99]
	v_cmp_ge_f32_e64 s[98:99], v243, v251
	v_cndmask_b32_e64 v24, 0, v196, s[100:101]
	v_cmp_ge_f32_e64 s[100:101], v244, v250
	v_cndmask_b32_e64 v9, 0, v197, vcc
	v_cmp_ge_f32_e32 vcc, v244, v251
	v_cndmask_b32_e64 v25, 0, v197, s[98:99]
	v_cmp_ge_f32_e64 s[98:99], v245, v250
	v_cndmask_b32_e64 v10, 0, v198, s[100:101]
	v_cmp_ge_f32_e64 s[100:101], v245, v251
	v_cndmask_b32_e64 v26, 0, v198, vcc
	v_cmp_ge_f32_e32 vcc, v246, v250
	v_cndmask_b32_e64 v11, 0, v199, s[98:99]
	v_cmp_ge_f32_e64 s[98:99], v246, v251
	v_cndmask_b32_e64 v27, 0, v199, s[100:101]
	v_cmp_ge_f32_e64 s[100:101], v247, v250
	v_cndmask_b32_e64 v12, 0, v200, vcc
	v_cmp_ge_f32_e32 vcc, v247, v251
	v_cndmask_b32_e64 v28, 0, v200, s[98:99]
	v_cmp_ge_f32_e64 s[98:99], v248, v250
	v_cndmask_b32_e64 v13, 0, v201, s[100:101]
	v_cmp_ge_f32_e64 s[100:101], v248, v251
	v_cndmask_b32_e64 v29, 0, v201, vcc
	v_cmp_ge_f32_e32 vcc, v249, v250
	v_cndmask_b32_e64 v14, 0, v202, s[98:99]
	v_cmp_ge_f32_e64 s[98:99], v249, v251
	v_cndmask_b32_e64 v30, 0, v202, s[100:101]
	v_cndmask_b32_e64 v15, 0, v203, vcc
	v_cndmask_b32_e64 v31, 0, v203, s[98:99]
	v_or3_b32 v0, v0, v1, v2
	v_or3_b32 v0, v0, v3, v4
	v_or3_b32 v0, v0, v5, v6
	v_or3_b32 v0, v0, v7, v8
	v_or3_b32 v0, v0, v9, v10
	v_or3_b32 v0, v0, v11, v12
	v_or3_b32 v0, v0, v13, v14
	v_or_b32_e32 v0, v0, v15
	v_or3_b32 v17, v17, v16, v18
	v_or3_b32 v17, v17, v19, v20
	v_or3_b32 v17, v17, v21, v22
	v_or3_b32 v17, v17, v23, v24
	v_or3_b32 v17, v17, v25, v26
	v_or3_b32 v17, v17, v27, v28
	v_or3_b32 v17, v17, v29, v30
	v_or_b32_e32 v17, v17, v31
	v_not_b32_e32 v16, v0
	v_and_b32_e32 v17, v17, v16
	s_waitcnt lgkmcnt(0)
	ds_write_b128 v223, v[234:237]
	ds_write_b128 v223, v[238:241] offset:1024
	ds_write_b128 v223, v[242:245] offset:2048
	ds_write_b128 v223, v[246:249] offset:3072
	v_add_u32_e32 v15, s6, v219
	s_branch .LBB0_830

; __device__ __forceinline__ int crow(int reg, int h) { return (reg & 3) + 8 * (reg >> 2) + 4 * h; }
; template <int STAGE>
; __device__ __forceinline__ void pass2(LAS unsigned char* lds, const bf16* kbase, int g, int t0, const bf16x8 (&qf)[4][4], const f32x4 lo4, const f32x4 hi4, int wave, int r, int h2) {
;     ...
;         f32x16 acc[4];
; #pragma unroll
;         for (int hd = 0; hd < 4; ++hd) {
;             acc[hd] = f32x16{};
; #pragma unroll
;             for (int s = 0; s < 4; ++s) acc[hd] = __builtin_amdgcn_mfma_f32_32x32x16_bf16(WN ? kn[s] : kf[s], qf[hd][s], acc[hd], 0, 0, 0);
;         }
;         const int zi = (8191 - 32 * kt) >> 7;
;         const int lim = tq - 32 * kt - 4 * h2;
;         unsigned gtw = 0u, eqw = 0u;
;         float svq[16];
; #pragma unroll
;         for (int rg = 0; rg < 16; ++rg) {
;             const int c0 = att::crow(rg, 0);
;             float sv = fsum4_s(__builtin_amdgcn_fmed3f(acc[0][rg], lo4.x, hi4.x), __builtin_amdgcn_fmed3f(acc[1][rg], lo4.y, hi4.y),
;                                __builtin_amdgcn_fmed3f(acc[2][rg], lo4.z, hi4.z), __builtin_amdgcn_fmed3f(acc[3][rg], lo4.w, hi4.w));
;             const int b = bin2(sv, zi);
.LBB0_840:
	s_cmp_lg_u32 s1, s64
	s_cbranch_scc0 .LBB0_853
	v_mfma_f32_32x32x16_bf16 v[0:15], v[156:159], v[64:67], 0
	s_lshl_b32 s1, s1, 5
	s_sub_i32 s6, 0x1fe0, s1
	s_lshr_b32 s6, s6, 7
	s_addk_i32 s6, 0xd0
	v_mfma_f32_32x32x16_bf16 v[16:31], v[156:159], v[80:83], 0
	v_mfma_f32_32x32x16_bf16 v[32:47], v[156:159], v[96:99], 0
	v_mfma_f32_32x32x16_bf16 v[48:63], v[156:159], v[112:115], 0
	v_mfma_f32_32x32x16_bf16 v[0:15], v[152:155], v[68:71], v[0:15]
	v_mfma_f32_32x32x16_bf16 v[16:31], v[152:155], v[84:87], v[16:31]
	v_mfma_f32_32x32x16_bf16 v[32:47], v[152:155], v[100:103], v[32:47]
	v_mfma_f32_32x32x16_bf16 v[48:63], v[152:155], v[116:119], v[48:63]
	v_mfma_f32_32x32x16_bf16 v[0:15], v[148:151], v[72:75], v[0:15]
	v_mfma_f32_32x32x16_bf16 v[16:31], v[148:151], v[88:91], v[16:31]
	v_mfma_f32_32x32x16_bf16 v[32:47], v[148:151], v[104:107], v[32:47]
	v_mfma_f32_32x32x16_bf16 v[48:63], v[148:151], v[120:123], v[48:63]
	v_mfma_f32_32x32x16_bf16 v[0:15], v[144:147], v[76:79], v[0:15]
	v_mfma_f32_32x32x16_bf16 v[16:31], v[144:147], v[92:95], v[16:31]
	v_mfma_f32_32x32x16_bf16 v[32:47], v[144:147], v[108:111], v[32:47]
	v_mfma_f32_32x32x16_bf16 v[48:63], v[144:147], v[124:127], v[48:63]
	v_cmp_gt_i32_e32 vcc, s6, v232
	v_cmp_ge_i32_e64 s[98:99], s6, v232
	s_nop 6
	v_cndmask_b32_e32 v250, v252, v177, vcc
	v_cndmask_b32_e64 v251, v253, v177, s[98:99]
	v_med3_f32 v0, v0, v207, v208
	v_med3_f32 v1, v1, v207, v208
	v_med3_f32 v2, v2, v207, v208
	v_med3_f32 v3, v3, v207, v208
	v_med3_f32 v4, v4, v207, v208
	v_med3_f32 v5, v5, v207, v208
	v_med3_f32 v6, v6, v207, v208
	v_med3_f32 v7, v7, v207, v208
	v_med3_f32 v8, v8, v207, v208
	v_med3_f32 v9, v9, v207, v208
	v_med3_f32 v10, v10, v207, v208
	v_med3_f32 v11, v11, v207, v208
	v_med3_f32 v12, v12, v207, v208
	v_med3_f32 v13, v13, v207, v208
	v_med3_f32 v14, v14, v207, v208
	v_med3_f32 v15, v15, v207, v208
	v_med3_f32 v16, v16, v209, v210
	v_med3_f32 v17, v17, v209, v210
	v_med3_f32 v18, v18, v209, v210
	v_med3_f32 v19, v19, v209, v210
	v_med3_f32 v20, v20, v209, v210
	v_med3_f32 v21, v21, v209, v210
	v_med3_f32 v22, v22, v209, v210
	v_med3_f32 v23, v23, v209, v210
	v_med3_f32 v24, v24, v209, v210
	v_med3_f32 v25, v25, v209, v210
	v_med3_f32 v26, v26, v209, v210
	v_med3_f32 v27, v27, v209, v210
	v_med3_f32 v28, v28, v209, v210
	v_med3_f32 v29, v29, v209, v210
	v_med3_f32 v30, v30, v209, v210
	v_med3_f32 v31, v31, v209, v210
	v_med3_f32 v32, v32, v212, v213
	v_med3_f32 v33, v33, v212, v213
	v_med3_f32 v34, v34, v212, v213
	v_med3_f32 v35, v35, v212, v213
	v_med3_f32 v36, v36, v212, v213
	v_med3_f32 v37, v37, v212, v213
	v_med3_f32 v38, v38, v212, v213
	v_med3_f32 v39, v39, v212, v213
	v_med3_f32 v40, v40, v212, v213
	v_med3_f32 v41, v41, v212, v213
	v_med3_f32 v42, v42, v212, v213
	v_med3_f32 v43, v43, v212, v213
	v_med3_f32 v44, v44, v212, v213
	v_med3_f32 v45, v45, v212, v213
	v_med3_f32 v46, v46, v212, v213
	v_med3_f32 v47, v47, v212, v213
	v_med3_f32 v48, v48, v214, v215
	v_med3_f32 v49, v49, v214, v215
	v_med3_f32 v50, v50, v214, v215
	v_med3_f32 v51, v51, v214, v215
	v_med3_f32 v52, v52, v214, v215
	v_med3_f32 v53, v53, v214, v215
	v_med3_f32 v54, v54, v214, v215
	v_med3_f32 v55, v55, v214, v215
	v_med3_f32 v56, v56, v214, v215
	v_med3_f32 v57, v57, v214, v215
	v_med3_f32 v58, v58, v214, v215
	v_med3_f32 v59, v59, v214, v215
	v_med3_f32 v60, v60, v214, v215
	v_med3_f32 v61, v61, v214, v215
	v_med3_f32 v62, v62, v214, v215
	v_med3_f32 v63, v63, v214, v215
	v_pk_add_f32 v[0:1], v[0:1], v[16:17]
	v_pk_add_f32 v[32:33], v[32:33], v[48:49]
	v_pk_add_f32 v[234:235], v[0:1], v[32:33]
	v_pk_add_f32 v[2:3], v[2:3], v[18:19]
	v_pk_add_f32 v[34:35], v[34:35], v[50:51]
	v_pk_add_f32 v[236:237], v[2:3], v[34:35]
	v_pk_add_f32 v[4:5], v[4:5], v[20:21]
	v_pk_add_f32 v[36:37], v[36:37], v[52:53]
	v_pk_add_f32 v[238:239], v[4:5], v[36:37]
; #define LAS __attribute__((address_space(3)))
; __device__ __forceinline__ int crow(int reg, int h) { return (reg & 3) + 8 * (reg >> 2) + 4 * h; }
; template <int STAGE>
; __device__ __forceinline__ void pass2(LAS unsigned char* lds, const bf16* kbase, int g, int t0, const bf16x8 (&qf)[4][4], const f32x4 lo4, const f32x4 hi4, int wave, int r, int h2) {
;     ...
;         for (int rg = 0; rg < 16; ++rg) {
;             const int c0 = att::crow(rg, 0);
;             float sv = fsum4_s(__builtin_amdgcn_fmed3f(acc[0][rg], lo4.x, hi4.x), __builtin_amdgcn_fmed3f(acc[1][rg], lo4.y, hi4.y),
;                                __builtin_amdgcn_fmed3f(acc[2][rg], lo4.z, hi4.z), __builtin_amdgcn_fmed3f(acc[3][rg], lo4.w, hi4.w));
;             const int b = bin2(sv, zi);
;             const bool valid = !DIAG || c0 <= lim;
;             if (STAGE == 0) {
;                 atomicAdd((unsigned*)&hist[r * HROW2 + (valid ? b : NB2)], 1u);
;             } else {
;                 if (valid && b > tb) gtw |= 1u << c0;
;                 if (valid && b == tb) eqw |= 1u << c0;
;                 svq[rg] = sv;
;             }
;         }
;         if (STAGE == 1) {
;             LAS unsigned char* st = lds + OFF2_SV + wave * 4096 + (r + 32 * h2) * 16;
; #pragma unroll
;             for (int q = 0; q < 4; ++q) *(LAS f32x4*)(st + q * 1024) = (f32x4){svq[4 * q], svq[4 * q + 1], svq[4 * q + 2], svq[4 * q + 3]};
	v_pk_add_f32 v[6:7], v[6:7], v[22:23]
	v_pk_add_f32 v[38:39], v[38:39], v[54:55]
	v_pk_add_f32 v[240:241], v[6:7], v[38:39]
	v_pk_add_f32 v[8:9], v[8:9], v[24:25]
	v_pk_add_f32 v[40:41], v[40:41], v[56:57]
	v_pk_add_f32 v[242:243], v[8:9], v[40:41]
	v_pk_add_f32 v[10:11], v[10:11], v[26:27]
	v_pk_add_f32 v[42:43], v[42:43], v[58:59]
	v_pk_add_f32 v[244:245], v[10:11], v[42:43]
	v_pk_add_f32 v[12:13], v[12:13], v[28:29]
	v_pk_add_f32 v[44:45], v[44:45], v[60:61]
	v_pk_add_f32 v[246:247], v[12:13], v[44:45]
	v_pk_add_f32 v[14:15], v[14:15], v[30:31]
	v_pk_add_f32 v[46:47], v[46:47], v[62:63]
	v_pk_add_f32 v[248:249], v[14:15], v[46:47]
	v_cmp_ge_f32_e32 vcc, v234, v250
	v_cmp_ge_f32_e64 s[98:99], v234, v251
	v_cmp_ge_f32_e64 s[100:101], v235, v250
	v_cndmask_b32_e64 v0, 0, 1, vcc
	v_cmp_ge_f32_e32 vcc, v235, v251
	v_cndmask_b32_e64 v16, 0, 1, s[98:99]
	v_cmp_ge_f32_e64 s[98:99], v236, v250
	v_cndmask_b32_e64 v1, 0, 2, s[100:101]
	v_cmp_ge_f32_e64 s[100:101], v236, v251
	v_cndmask_b32_e64 v17, 0, 2, vcc
	v_cmp_ge_f32_e32 vcc, v237, v250
	v_cndmask_b32_e64 v2, 0, 4, s[98:99]
	v_cmp_ge_f32_e64 s[98:99], v237, v251
	v_cndmask_b32_e64 v18, 0, 4, s[100:101]
	v_cmp_ge_f32_e64 s[100:101], v238, v250
	v_cndmask_b32_e64 v3, 0, 8, vcc
	v_cmp_ge_f32_e32 vcc, v238, v251
	v_cndmask_b32_e64 v19, 0, 8, s[98:99]
	v_cmp_ge_f32_e64 s[98:99], v239, v250
	v_cndmask_b32_e64 v4, 0, v186, s[100:101]
	v_cmp_ge_f32_e64 s[100:101], v239, v251
	v_cndmask_b32_e64 v20, 0, v186, vcc
	v_cmp_ge_f32_e32 vcc, v240, v250
	v_cndmask_b32_e64 v5, 0, v193, s[98:99]
	v_cmp_ge_f32_e64 s[98:99], v240, v251
	v_cndmask_b32_e64 v21, 0, v193, s[100:101]
	v_cmp_ge_f32_e64 s[100:101], v241, v250
	v_cndmask_b32_e64 v6, 0, v194, vcc
	v_cmp_ge_f32_e32 vcc, v241, v251
	v_cndmask_b32_e64 v22, 0, v194, s[98:99]
	v_cmp_ge_f32_e64 s[98:99], v242, v250
	v_cndmask_b32_e64 v7, 0, v195, s[100:101]
	v_cmp_ge_f32_e64 s[100:101], v242, v251
	v_cndmask_b32_e64 v23, 0, v195, vcc
	v_cmp_ge_f32_e32 vcc, v243, v250
	v_cndmask_b32_e64 v8, 0, v196, s[98:99]
	v_cmp_ge_f32_e64 s[98:99], v243, v251
	v_cndmask_b32_e64 v24, 0, v196, s[100:101]
	v_cmp_ge_f32_e64 s[100:101], v244, v250
	v_cndmask_b32_e64 v9, 0, v197, vcc
	v_cmp_ge_f32_e32 vcc, v244, v251
	v_cndmask_b32_e64 v25, 0, v197, s[98:99]
	v_cmp_ge_f32_e64 s[98:99], v245, v250
	v_cndmask_b32_e64 v10, 0, v198, s[100:101]
	v_cmp_ge_f32_e64 s[100:101], v245, v251
	v_cndmask_b32_e64 v26, 0, v198, vcc
	v_cmp_ge_f32_e32 vcc, v246, v250
	v_cndmask_b32_e64 v11, 0, v199, s[98:99]
	v_cmp_ge_f32_e64 s[98:99], v246, v251
	v_cndmask_b32_e64 v27, 0, v199, s[100:101]
	v_cmp_ge_f32_e64 s[100:101], v247, v250
	v_cndmask_b32_e64 v12, 0, v200, vcc
	v_cmp_ge_f32_e32 vcc, v247, v251
	v_cndmask_b32_e64 v28, 0, v200, s[98:99]
	v_cmp_ge_f32_e64 s[98:99], v248, v250
	v_cndmask_b32_e64 v13, 0, v201, s[100:101]
	v_cmp_ge_f32_e64 s[100:101], v248, v251
	v_cndmask_b32_e64 v29, 0, v201, vcc
	v_cmp_ge_f32_e32 vcc, v249, v250
	v_cndmask_b32_e64 v14, 0, v202, s[98:99]
	v_cmp_ge_f32_e64 s[98:99], v249, v251
	v_cndmask_b32_e64 v30, 0, v202, s[100:101]
	v_cndmask_b32_e64 v15, 0, v203, vcc
	v_cndmask_b32_e64 v31, 0, v203, s[98:99]
	v_or3_b32 v0, v0, v1, v2
	v_or3_b32 v0, v0, v3, v4
	v_or3_b32 v0, v0, v5, v6
	v_or3_b32 v0, v0, v7, v8
	v_or3_b32 v0, v0, v9, v10
	v_or3_b32 v0, v0, v11, v12
	v_or3_b32 v0, v0, v13, v14
	v_or_b32_e32 v0, v0, v15
	v_or3_b32 v17, v17, v16, v18
	v_or3_b32 v17, v17, v19, v20
	v_or3_b32 v17, v17, v21, v22
	v_or3_b32 v17, v17, v23, v24
	v_or3_b32 v17, v17, v25, v26
	v_or3_b32 v17, v17, v27, v28
	v_or3_b32 v17, v17, v29, v30
	v_or_b32_e32 v17, v17, v31
	v_not_b32_e32 v16, v0
	v_and_b32_e32 v17, v17, v16
	s_waitcnt lgkmcnt(0)
	ds_write_b128 v223, v[234:237]
	ds_write_b128 v223, v[238:241] offset:1024
	ds_write_b128 v223, v[242:245] offset:2048
	ds_write_b128 v223, v[246:249] offset:3072
	v_add_u32_e32 v15, s1, v219
	s_branch .LBB0_844
